# v23_finalhoist
# speedup vs baseline: 1.0173x; 1.0013x over previous
_Z7k_finalPKdPf:
	s_load_dwordx2 s[2:3], s[0:1], 0x0
	v_lshrrev_b32_e32 v6, 1, v0
	v_and_b32_e32 v7, 1, v0
	v_lshlrev_b32_e32 v0, 10, v6
	v_mov_b32_e32 v1, 0
	s_load_dwordx2 s[24:25], s[0:1], 0x8
	s_waitcnt lgkmcnt(0)
	s_load_dwordx16 s[8:23], s[2:3], 0x200
	v_lshl_add_u64 v[2:3], s[2:3], 0, v[0:1]
	v_lshlrev_b32_e32 v0, 3, v7
	v_lshl_add_u64 v[2:3], v[2:3], 0, v[0:1]
	global_load_dwordx2 v[4:5], v[2:3], off offset:1024
	global_load_dwordx2 v[8:9], v[2:3], off offset:1088
	global_load_dwordx2 v[10:11], v[2:3], off offset:1040
	global_load_dwordx2 v[12:13], v[2:3], off offset:1056
	global_load_dwordx2 v[14:15], v[2:3], off offset:1072
	global_load_dwordx2 v[16:17], v[2:3], off offset:1104
	global_load_dwordx2 v[18:19], v[2:3], off offset:1120
	global_load_dwordx2 v[20:21], v[2:3], off offset:1136
	global_load_dwordx2 v[22:23], v[2:3], off offset:1152
	global_load_dwordx2 v[24:25], v[2:3], off offset:1168
	global_load_dwordx2 v[26:27], v[2:3], off offset:1184
	global_load_dwordx2 v[28:29], v[2:3], off offset:1200
	global_load_dwordx2 v[30:31], v[2:3], off offset:1216
	global_load_dwordx2 v[32:33], v[2:3], off offset:1232
	global_load_dwordx2 v[34:35], v[2:3], off offset:1248
	global_load_dwordx2 v[36:37], v[2:3], off offset:1264
	global_load_dwordx2 v[38:39], v[2:3], off offset:1280
	global_load_dwordx2 v[40:41], v[2:3], off offset:1296
	global_load_dwordx2 v[42:43], v[2:3], off offset:1312
	global_load_dwordx2 v[44:45], v[2:3], off offset:1328
	global_load_dwordx2 v[46:47], v[2:3], off offset:1344
	global_load_dwordx2 v[48:49], v[2:3], off offset:1360
	global_load_dwordx2 v[50:51], v[2:3], off offset:1376
	global_load_dwordx2 v[52:53], v[2:3], off offset:1392
	v_mbcnt_lo_u32_b32 v0, -1, 0
	v_mbcnt_hi_u32_b32 v0, -1, v0
	s_waitcnt vmcnt(23)
	v_add_f64 v[4:5], v[4:5], 0
	s_waitcnt vmcnt(22)
	v_add_f64 v[4:5], v[4:5], v[8:9]
	global_load_dwordx2 v[8:9], v[2:3], off offset:1408
	global_load_dwordx2 v[54:55], v[2:3], off offset:1424
	global_load_dwordx2 v[56:57], v[2:3], off offset:1440
	global_load_dwordx2 v[58:59], v[2:3], off offset:1456
	s_waitcnt vmcnt(25)
	v_add_f64 v[10:11], v[10:11], 0
	s_waitcnt vmcnt(24)
	v_add_f64 v[12:13], v[12:13], 0
	s_waitcnt vmcnt(23)
	v_add_f64 v[14:15], v[14:15], 0
	s_waitcnt vmcnt(22)
	v_add_f64 v[10:11], v[10:11], v[16:17]
	s_waitcnt vmcnt(21)
	v_add_f64 v[12:13], v[12:13], v[18:19]
	s_waitcnt vmcnt(20)
	v_add_f64 v[14:15], v[14:15], v[20:21]
	s_waitcnt vmcnt(19)
	v_add_f64 v[4:5], v[4:5], v[22:23]
	global_load_dwordx2 v[16:17], v[2:3], off offset:1472
	global_load_dwordx2 v[18:19], v[2:3], off offset:1488
	global_load_dwordx2 v[20:21], v[2:3], off offset:1504
	global_load_dwordx2 v[22:23], v[2:3], off offset:1520
	s_waitcnt vmcnt(22)
	v_add_f64 v[10:11], v[10:11], v[24:25]
	s_waitcnt vmcnt(21)
	v_add_f64 v[12:13], v[12:13], v[26:27]
	s_waitcnt vmcnt(20)
	v_add_f64 v[14:15], v[14:15], v[28:29]
	s_waitcnt vmcnt(19)
	v_add_f64 v[4:5], v[4:5], v[30:31]
	global_load_dwordx2 v[24:25], v[2:3], off offset:1536
	global_load_dwordx2 v[26:27], v[2:3], off offset:1552
	global_load_dwordx2 v[28:29], v[2:3], off offset:1568
	global_load_dwordx2 v[30:31], v[2:3], off offset:1584
	s_waitcnt vmcnt(22)
	v_add_f64 v[10:11], v[10:11], v[32:33]
	s_waitcnt vmcnt(21)
	v_add_f64 v[12:13], v[12:13], v[34:35]
	s_waitcnt vmcnt(20)
	v_add_f64 v[14:15], v[14:15], v[36:37]
	s_waitcnt vmcnt(19)
	v_add_f64 v[4:5], v[4:5], v[38:39]
	global_load_dwordx2 v[32:33], v[2:3], off offset:1600
	global_load_dwordx2 v[34:35], v[2:3], off offset:1616
	global_load_dwordx2 v[36:37], v[2:3], off offset:1632
	global_load_dwordx2 v[38:39], v[2:3], off offset:1648
	s_waitcnt vmcnt(22)
	v_add_f64 v[10:11], v[10:11], v[40:41]
	s_waitcnt vmcnt(21)
	v_add_f64 v[12:13], v[12:13], v[42:43]
	s_waitcnt vmcnt(20)
	v_add_f64 v[14:15], v[14:15], v[44:45]
	s_waitcnt vmcnt(19)
	v_add_f64 v[4:5], v[4:5], v[46:47]
	global_load_dwordx2 v[40:41], v[2:3], off offset:1664
	global_load_dwordx2 v[42:43], v[2:3], off offset:1680
	global_load_dwordx2 v[44:45], v[2:3], off offset:1696
	global_load_dwordx2 v[46:47], v[2:3], off offset:1712
	s_waitcnt vmcnt(22)
	v_add_f64 v[10:11], v[10:11], v[48:49]
	s_waitcnt vmcnt(21)
	v_add_f64 v[12:13], v[12:13], v[50:51]
	s_waitcnt vmcnt(20)
	v_add_f64 v[14:15], v[14:15], v[52:53]
	s_waitcnt vmcnt(19)
	v_add_f64 v[4:5], v[4:5], v[8:9]
	global_load_dwordx2 v[8:9], v[2:3], off offset:1728
	global_load_dwordx2 v[48:49], v[2:3], off offset:1744
	global_load_dwordx2 v[50:51], v[2:3], off offset:1760
	global_load_dwordx2 v[52:53], v[2:3], off offset:1776
	s_waitcnt vmcnt(22)
	v_add_f64 v[10:11], v[10:11], v[54:55]
	s_waitcnt vmcnt(21)
	v_add_f64 v[12:13], v[12:13], v[56:57]
	s_waitcnt vmcnt(20)
	v_add_f64 v[14:15], v[14:15], v[58:59]
	s_waitcnt vmcnt(19)
	v_add_f64 v[4:5], v[4:5], v[16:17]
	s_waitcnt vmcnt(18)
	v_add_f64 v[10:11], v[10:11], v[18:19]
	s_waitcnt vmcnt(17)
	v_add_f64 v[12:13], v[12:13], v[20:21]
	s_waitcnt vmcnt(16)
	v_add_f64 v[14:15], v[14:15], v[22:23]
	s_waitcnt vmcnt(15)
	v_add_f64 v[4:5], v[4:5], v[24:25]
	s_waitcnt vmcnt(14)
	v_add_f64 v[10:11], v[10:11], v[26:27]
	s_waitcnt vmcnt(13)
	v_add_f64 v[12:13], v[12:13], v[28:29]
	s_waitcnt vmcnt(12)
	v_add_f64 v[14:15], v[14:15], v[30:31]
	s_waitcnt vmcnt(11)
	v_add_f64 v[4:5], v[4:5], v[32:33]
	s_waitcnt vmcnt(10)
	v_add_f64 v[10:11], v[10:11], v[34:35]
	s_waitcnt vmcnt(9)
	v_add_f64 v[12:13], v[12:13], v[36:37]
	s_waitcnt vmcnt(8)
	v_add_f64 v[14:15], v[14:15], v[38:39]
	global_load_dwordx2 v[16:17], v[2:3], off offset:1792
	global_load_dwordx2 v[18:19], v[2:3], off offset:1808
	global_load_dwordx2 v[20:21], v[2:3], off offset:1824
	global_load_dwordx2 v[22:23], v[2:3], off offset:1840
	global_load_dwordx2 v[24:25], v[2:3], off offset:1856
	global_load_dwordx2 v[26:27], v[2:3], off offset:1872
	global_load_dwordx2 v[28:29], v[2:3], off offset:1888
	global_load_dwordx2 v[30:31], v[2:3], off offset:1904
	global_load_dwordx2 v[32:33], v[2:3], off offset:1920
	global_load_dwordx2 v[34:35], v[2:3], off offset:1936
	global_load_dwordx2 v[36:37], v[2:3], off offset:1952
	global_load_dwordx2 v[38:39], v[2:3], off offset:1968
	global_load_dwordx2 v[54:55], v[2:3], off offset:1984
	global_load_dwordx2 v[56:57], v[2:3], off offset:2000
	global_load_dwordx2 v[58:59], v[2:3], off offset:2016
	s_nop 0
	global_load_dwordx2 v[2:3], v[2:3], off offset:2032
	s_waitcnt vmcnt(23)
	v_add_f64 v[4:5], v[4:5], v[40:41]
	s_waitcnt vmcnt(22)
	v_add_f64 v[10:11], v[10:11], v[42:43]
	s_waitcnt vmcnt(21)
	v_add_f64 v[12:13], v[12:13], v[44:45]
	s_waitcnt vmcnt(20)
	v_add_f64 v[14:15], v[14:15], v[46:47]
	s_waitcnt vmcnt(19)
	v_add_f64 v[4:5], v[4:5], v[8:9]
	s_waitcnt vmcnt(18)
	v_add_f64 v[8:9], v[10:11], v[48:49]
	s_waitcnt vmcnt(17)
	v_add_f64 v[10:11], v[12:13], v[50:51]
	s_waitcnt vmcnt(16)
	v_add_f64 v[12:13], v[14:15], v[52:53]
	s_waitcnt vmcnt(15)
	v_add_f64 v[4:5], v[4:5], v[16:17]
	s_waitcnt vmcnt(14)
	v_add_f64 v[8:9], v[8:9], v[18:19]
	s_waitcnt vmcnt(13)
	v_add_f64 v[10:11], v[10:11], v[20:21]
	s_waitcnt vmcnt(12)
	v_add_f64 v[12:13], v[12:13], v[22:23]
	s_waitcnt vmcnt(11)
	v_add_f64 v[4:5], v[4:5], v[24:25]
	s_waitcnt vmcnt(10)
	v_add_f64 v[8:9], v[8:9], v[26:27]
	s_waitcnt vmcnt(9)
	v_add_f64 v[10:11], v[10:11], v[28:29]
	s_waitcnt vmcnt(8)
	v_add_f64 v[12:13], v[12:13], v[30:31]
	s_waitcnt vmcnt(7)
	v_add_f64 v[4:5], v[4:5], v[32:33]
	s_waitcnt vmcnt(6)
	v_add_f64 v[8:9], v[8:9], v[34:35]
	s_waitcnt vmcnt(5)
	v_add_f64 v[10:11], v[10:11], v[36:37]
	s_waitcnt vmcnt(4)
	v_add_f64 v[12:13], v[12:13], v[38:39]
	s_waitcnt vmcnt(3)
	v_add_f64 v[4:5], v[4:5], v[54:55]
	s_waitcnt vmcnt(2)
	v_add_f64 v[8:9], v[8:9], v[56:57]
	s_waitcnt vmcnt(1)
	v_add_f64 v[10:11], v[10:11], v[58:59]
	s_waitcnt vmcnt(0)
	v_add_f64 v[2:3], v[12:13], v[2:3]
	v_add_f64 v[4:5], v[8:9], v[4:5]
	v_add_f64 v[2:3], v[2:3], v[10:11]
	v_add_f64 v[4:5], v[2:3], v[4:5]
	v_and_b32_e32 v3, 64, v0
	v_xor_b32_e32 v2, 1, v0
	v_add_u32_e32 v3, 64, v3
	v_cmp_lt_i32_e32 vcc, v2, v3
	s_nop 1
	v_cndmask_b32_e32 v0, v0, v2, vcc
	v_lshlrev_b32_e32 v0, 2, v0
	ds_bpermute_b32 v2, v0, v4
	ds_bpermute_b32 v3, v0, v5
	v_cmp_eq_u32_e32 vcc, 0, v7
	s_and_saveexec_b64 s[4:5], vcc
	s_cbranch_execz .LBB5_2
	v_mov_b32_e32 v8, 0x5ed9812d
	v_mov_b32_e32 v9, 0x4138f40b
	v_fmac_f64_e32 v[8:9], 0xc0700000, v[4:5]
	s_waitcnt lgkmcnt(0)
	v_add_f64 v[4:5], s[8:9], 0
	v_add_f64 v[4:5], v[4:5], s[10:11]
	v_add_f64 v[4:5], v[4:5], s[12:13]
	v_add_f64 v[4:5], v[4:5], s[14:15]
	v_add_f64 v[4:5], v[4:5], s[16:17]
	v_add_f64 v[4:5], v[4:5], s[18:19]
	v_add_f64 v[4:5], v[4:5], s[20:21]
	v_add_f64 v[4:5], v[4:5], s[22:23]
	v_ldexp_f64 v[4:5], -v[4:5], 9
	v_lshlrev_b32_e32 v0, 2, v6
	v_fmac_f64_e32 v[4:5], 0.5, v[2:3]
	v_lshl_add_u64 v[0:1], s[24:25], 0, v[0:1]
	v_add_f64 v[2:3], v[8:9], v[4:5]
	v_add_co_u32_e32 v0, vcc, 0x4000000, v0
	v_cvt_f32_f64_e32 v2, v[2:3]
	s_nop 0
	v_addc_co_u32_e32 v1, vcc, 0, v1, vcc
	global_store_dword v[0:1], v2, off

	.amdhsa_kernel _Z7k_finalPKdPf
		.amdhsa_group_segment_fixed_size 0
		.amdhsa_private_segment_fixed_size 0
		.amdhsa_kernarg_size 16
		.amdhsa_user_sgpr_count 2
		.amdhsa_user_sgpr_dispatch_ptr 0
		.amdhsa_user_sgpr_queue_ptr 0
		.amdhsa_user_sgpr_kernarg_segment_ptr 1
		.amdhsa_user_sgpr_dispatch_id 0
		.amdhsa_user_sgpr_kernarg_preload_length 0
		.amdhsa_user_sgpr_kernarg_preload_offset 0
		.amdhsa_user_sgpr_private_segment_size 0
		.amdhsa_uses_dynamic_stack 0
		.amdhsa_enable_private_segment 0
		.amdhsa_system_sgpr_workgroup_id_x 1
		.amdhsa_system_sgpr_workgroup_id_y 0
		.amdhsa_system_sgpr_workgroup_id_z 0
		.amdhsa_system_sgpr_workgroup_info 0
		.amdhsa_system_vgpr_workitem_id 0
		.amdhsa_next_free_vgpr 60
		.amdhsa_next_free_sgpr 26
		.amdhsa_accum_offset 60
		.amdhsa_reserve_vcc 1
		.amdhsa_float_round_mode_32 0
		.amdhsa_float_round_mode_16_64 0
		.amdhsa_float_denorm_mode_32 3
		.amdhsa_float_denorm_mode_16_64 3
		.amdhsa_dx10_clamp 1
		.amdhsa_ieee_mode 1
		.amdhsa_fp16_overflow 0
		.amdhsa_tg_split 0
		.amdhsa_exception_fp_ieee_invalid_op 0
		.amdhsa_exception_fp_denorm_src 0
		.amdhsa_exception_fp_ieee_div_zero 0
		.amdhsa_exception_fp_ieee_overflow 0
		.amdhsa_exception_fp_ieee_underflow 0
		.amdhsa_exception_fp_ieee_inexact 0
		.amdhsa_exception_int_div_zero 0
	.end_amdhsa_kernel

amdhsa.kernels:
  - .agpr_count:     16
    .args:
      - .actual_access:  read_only
        .address_space:  global
        .offset:         0
        .size:           8
        .value_kind:     global_buffer
      - .actual_access:  read_only
        .address_space:  global
        .offset:         8
        .size:           8
        .value_kind:     global_buffer
      - .actual_access:  read_only
        .address_space:  global
        .offset:         16
        .size:           8
        .value_kind:     global_buffer
      - .actual_access:  write_only
        .address_space:  global
        .offset:         24
        .size:           8
        .value_kind:     global_buffer
      - .actual_access:  write_only
        .address_space:  global
        .offset:         32
        .size:           8
        .value_kind:     global_buffer
      - .actual_access:  write_only
        .address_space:  global
        .offset:         40
        .size:           8
        .value_kind:     global_buffer
    .group_segment_fixed_size: 18944
    .kernarg_segment_align: 8
    .kernarg_segment_size: 48
    .language:       OpenCL C
    .language_version:
      - 2
      - 0
    .max_flat_workgroup_size: 256
    .name:           _Z9k_gemm_byPKfS0_S0_PfS1_Pd
    .private_segment_fixed_size: 0
    .sgpr_count:     22
    .sgpr_spill_count: 0
    .symbol:         _Z9k_gemm_byPKfS0_S0_PfS1_Pd.kd
    .uniform_work_group_size: 1
    .uses_dynamic_stack: false
    .vgpr_count:     168
    .vgpr_spill_count: 0
    .wavefront_size: 64
  - .agpr_count:     48
    .args:
      - .address_space:  global
        .offset:         0
        .size:           8
        .value_kind:     global_buffer
      - .address_space:  global
        .offset:         8
        .size:           8
        .value_kind:     global_buffer
      - .address_space:  global
        .offset:         16
        .size:           8
        .value_kind:     global_buffer
      - .address_space:  global
        .offset:         24
        .size:           8
        .value_kind:     global_buffer
      - .actual_access:  write_only
        .address_space:  global
        .offset:         32
        .size:           8
        .value_kind:     global_buffer
      - .offset:         40
        .size:           4
        .value_kind:     by_value
      - .actual_access:  read_only
        .address_space:  global
        .offset:         48
        .size:           8
        .value_kind:     global_buffer
      - .actual_access:  read_only
        .address_space:  global
        .offset:         56
        .size:           8
        .value_kind:     global_buffer
      - .actual_access:  read_only
        .address_space:  global
        .offset:         64
        .size:           8
        .value_kind:     global_buffer
      - .address_space:  global
        .offset:         72
        .size:           8
        .value_kind:     global_buffer
      - .offset:         80
        .size:           4
        .value_kind:     by_value
      - .actual_access:  write_only
        .address_space:  global
        .offset:         88
        .size:           8
        .value_kind:     global_buffer
      - .actual_access:  write_only
        .address_space:  global
        .offset:         96
        .size:           8
        .value_kind:     global_buffer
      - .actual_access:  write_only
        .address_space:  global
        .offset:         104
        .size:           8
        .value_kind:     global_buffer
    .group_segment_fixed_size: 139520
    .kernarg_segment_align: 8
    .kernarg_segment_size: 112
    .language:       OpenCL C
    .language_version:
      - 2
      - 0
    .max_flat_workgroup_size: 256
    .name:           _Z7k_chol2PfS_S_S_PdiPKfS2_S2_S_iS_PDF16_S_
    .private_segment_fixed_size: 0
    .sgpr_count:     106
    .sgpr_spill_count: 0
    .symbol:         _Z7k_chol2PfS_S_S_PdiPKfS2_S2_S_iS_PDF16_S_.kd
    .uniform_work_group_size: 1
    .uses_dynamic_stack: false
    .vgpr_count:     252
    .vgpr_spill_count: 0
    .wavefront_size: 64
  - .agpr_count:     16
    .args:
      - .actual_access:  read_only
        .address_space:  global
        .offset:         0
        .size:           8
        .value_kind:     global_buffer
      - .address_space:  global
        .offset:         8
        .size:           8
        .value_kind:     global_buffer
      - .address_space:  global
        .offset:         16
        .size:           8
        .value_kind:     global_buffer
      - .actual_access:  read_only
        .address_space:  global
        .offset:         24
        .size:           8
        .value_kind:     global_buffer
      - .actual_access:  write_only
        .address_space:  global
        .offset:         32
        .size:           8
        .value_kind:     global_buffer
      - .actual_access:  write_only
        .address_space:  global
        .offset:         40
        .size:           8
        .value_kind:     global_buffer
      - .actual_access:  write_only
        .address_space:  global
        .offset:         48
        .size:           8
        .value_kind:     global_buffer
    .group_segment_fixed_size: 79872
    .kernarg_segment_align: 8
    .kernarg_segment_size: 56
    .language:       OpenCL C
    .language_version:
      - 2
      - 0
    .max_flat_workgroup_size: 256
    .name:           _Z6k_tailPKfPfS1_S0_S1_PDF16_S1_
    .private_segment_fixed_size: 0
    .sgpr_count:     34
    .sgpr_spill_count: 0
    .symbol:         _Z6k_tailPKfPfS1_S0_S1_PDF16_S1_.kd
    .uniform_work_group_size: 1
    .uses_dynamic_stack: false
    .vgpr_count:     160
    .vgpr_spill_count: 0
    .wavefront_size: 64
  - .agpr_count:     0
    .args:
      - .actual_access:  read_only
        .address_space:  global
        .offset:         0
        .size:           8
        .value_kind:     global_buffer
      - .actual_access:  read_only
        .address_space:  global
        .offset:         8
        .size:           8
        .value_kind:     global_buffer
      - .actual_access:  read_only
        .address_space:  global
        .offset:         16
        .size:           8
        .value_kind:     global_buffer
      - .actual_access:  write_only
        .address_space:  global
        .offset:         24
        .size:           8
        .value_kind:     global_buffer
      - .actual_access:  write_only
        .address_space:  global
        .offset:         32
        .size:           8
        .value_kind:     global_buffer
      - .actual_access:  write_only
        .address_space:  global
        .offset:         40
        .size:           8
        .value_kind:     global_buffer
    .group_segment_fixed_size: 16896
    .kernarg_segment_align: 8
    .kernarg_segment_size: 48
    .language:       OpenCL C
    .language_version:
      - 2
      - 0
    .max_flat_workgroup_size: 256
    .name:           _Z6k_prepPKfS0_S0_PfPDF16_S1_
    .private_segment_fixed_size: 0
    .sgpr_count:     28
    .sgpr_spill_count: 0
    .symbol:         _Z6k_prepPKfS0_S0_PfPDF16_S1_.kd
    .uniform_work_group_size: 1
    .uses_dynamic_stack: false
    .vgpr_count:     150
    .vgpr_spill_count: 0
    .wavefront_size: 64
  - .agpr_count:     0
    .args:
      - .actual_access:  read_only
        .address_space:  global
        .offset:         0
        .size:           8
        .value_kind:     global_buffer
      - .actual_access:  read_only
        .address_space:  global
        .offset:         8
        .size:           8
        .value_kind:     global_buffer
      - .actual_access:  read_only
        .address_space:  global
        .offset:         16
        .size:           8
        .value_kind:     global_buffer
      - .actual_access:  read_only
        .address_space:  global
        .offset:         24
        .size:           8
        .value_kind:     global_buffer
      - .actual_access:  write_only
        .address_space:  global
        .offset:         32
        .size:           8
        .value_kind:     global_buffer
      - .actual_access:  write_only
        .address_space:  global
        .offset:         40
        .size:           8
        .value_kind:     global_buffer
    .group_segment_fixed_size: 111616
    .kernarg_segment_align: 8
    .kernarg_segment_size: 48
    .language:       OpenCL C
    .language_version:
      - 2
      - 0
    .max_flat_workgroup_size: 512
    .name:           _Z6k_mainPKfS0_PKDF16_S0_PfPd
    .private_segment_fixed_size: 0
    .sgpr_count:     25
    .sgpr_spill_count: 0
    .symbol:         _Z6k_mainPKfS0_PKDF16_S0_PfPd.kd
    .uniform_work_group_size: 1
    .uses_dynamic_stack: false
    .vgpr_count:     248
    .vgpr_spill_count: 0
    .wavefront_size: 64
  - .agpr_count:     0
    .args:
      - .actual_access:  read_only
        .address_space:  global
        .offset:         0
        .size:           8
        .value_kind:     global_buffer
      - .actual_access:  write_only
        .address_space:  global
        .offset:         8
        .size:           8
        .value_kind:     global_buffer
    .group_segment_fixed_size: 0
    .kernarg_segment_align: 8
    .kernarg_segment_size: 16
    .language:       OpenCL C
    .language_version:
      - 2
      - 0
    .max_flat_workgroup_size: 1024
    .name:           _Z7k_finalPKdPf
    .private_segment_fixed_size: 0
    .sgpr_count:     32
    .sgpr_spill_count: 0
    .symbol:         _Z7k_finalPKdPf.kd
    .uniform_work_group_size: 1
    .uses_dynamic_stack: false
    .vgpr_count:     60
    .vgpr_spill_count: 0
    .wavefront_size: 64
